# v6_prep_qbias
# speedup vs baseline: 1.0588x; 1.0112x over previous
.LBB0_61:
	s_waitcnt lgkmcnt(0)
	global_load_dword v24, v12, s[4:5]
	global_load_dword v25, v12, s[4:5] offset:512
	global_load_dword v26, v12, s[4:5] offset:1024
	global_load_dword v9, v12, s[6:7]

.LBB0_64:
.LBB0_65:
	s_waitcnt lgkmcnt(0)
	global_load_dword v27, v12, s[4:5] offset:4
	global_load_dword v28, v12, s[4:5] offset:516
	global_load_dword v29, v12, s[4:5] offset:1028
	global_load_dword v11, v12, s[6:7] offset:4

.LBB0_68:
.LBB0_69:
	s_waitcnt lgkmcnt(0)
	global_load_dword v30, v12, s[4:5] offset:8
	global_load_dword v31, v12, s[4:5] offset:520
	global_load_dword v32, v12, s[4:5] offset:1032
	global_load_dword v14, v12, s[6:7] offset:8

.LBB0_72:
.LBB0_73:
	s_waitcnt lgkmcnt(0)
	global_load_dword v33, v12, s[4:5] offset:12
	global_load_dword v34, v12, s[4:5] offset:524
	global_load_dword v35, v12, s[4:5] offset:1036
	global_load_dword v16, v12, s[6:7] offset:12

.LBB0_76:
.LBB0_77:
	s_waitcnt lgkmcnt(0)
	global_load_dword v36, v12, s[4:5] offset:16
	global_load_dword v37, v12, s[4:5] offset:528
	global_load_dword v38, v12, s[4:5] offset:1040
	global_load_dword v18, v12, s[6:7] offset:16

.LBB0_80:
.LBB0_81:
	s_waitcnt lgkmcnt(0)
	global_load_dword v39, v12, s[4:5] offset:20
	global_load_dword v40, v12, s[4:5] offset:532
	global_load_dword v41, v12, s[4:5] offset:1044
	global_load_dword v20, v12, s[6:7] offset:20

.LBB0_84:
.LBB0_85:
	s_waitcnt lgkmcnt(0)
	global_load_dword v42, v12, s[4:5] offset:24
	global_load_dword v43, v12, s[4:5] offset:536
	global_load_dword v44, v12, s[4:5] offset:1048
	global_load_dword v5, v12, s[6:7] offset:24

.LBB0_88:
.LBB0_89:
	v_lshlrev_b32_e32 v12, 2, v7
	s_waitcnt lgkmcnt(0)
	global_load_dword v45, v12, s[4:5]
	global_load_dword v46, v12, s[4:5] offset:512
	global_load_dword v47, v12, s[4:5] offset:1024
	global_load_dword v8, v12, s[6:7]
.LBB0_90:
	v_mov_b32_e32 v23, 0
	v_lshlrev_b32_e32 v22, 6, v7
	v_lshl_add_u64 v[2:3], v[2:3], 0, v[22:23]
	global_load_dword v2, v[2:3], off
	s_and_b64 vcc, exec, s[0:1]
	s_cbranch_vccz .Lqb_done
	s_waitcnt vmcnt(0)
	v_add_f32_e32 v24, v24, v25
	v_add_f32_e32 v24, v24, v26
	v_fmac_f32_e32 v9, 0.5, v24
	v_add_f32_e32 v27, v27, v28
	v_add_f32_e32 v27, v27, v29
	v_fmac_f32_e32 v11, 0.5, v27
	v_add_f32_e32 v30, v30, v31
	v_add_f32_e32 v30, v30, v32
	v_fmac_f32_e32 v14, 0.5, v30
	v_add_f32_e32 v33, v33, v34
	v_add_f32_e32 v33, v33, v35
	v_fmac_f32_e32 v16, 0.5, v33
	v_add_f32_e32 v36, v36, v37
	v_add_f32_e32 v36, v36, v38
	v_fmac_f32_e32 v18, 0.5, v36
	v_add_f32_e32 v39, v39, v40
	v_add_f32_e32 v39, v39, v41
	v_fmac_f32_e32 v20, 0.5, v39
	v_add_f32_e32 v42, v42, v43
	v_add_f32_e32 v42, v42, v44
	v_fmac_f32_e32 v5, 0.5, v42
	v_add_f32_e32 v45, v45, v46
	v_add_f32_e32 v45, v45, v47
	v_fmac_f32_e32 v8, 0.5, v45
.Lqb_done:
	s_waitcnt vmcnt(7)
	v_fma_f32 v3, v9, v10, 0
	s_waitcnt vmcnt(6)
	v_fmac_f32_e32 v3, v11, v13
	s_waitcnt vmcnt(5)
	v_fmac_f32_e32 v3, v14, v15
	s_waitcnt vmcnt(4)
	v_fmac_f32_e32 v3, v16, v17
	s_waitcnt vmcnt(3)
	v_fmac_f32_e32 v3, v18, v19
	s_waitcnt vmcnt(2)
	v_fmac_f32_e32 v3, v20, v6
	s_waitcnt vmcnt(1)
	v_fmac_f32_e32 v3, v5, v4
	v_cmp_gt_u32_e32 vcc, 16, v0
	s_waitcnt vmcnt(0)
	v_fmac_f32_e32 v3, v8, v2
	ds_write_b32 v1, v3
	s_waitcnt lgkmcnt(0)
	s_barrier
	s_and_saveexec_b64 s[0:1], vcc
	s_cbranch_execz .LBB0_92
	ds_read2_b32 v[2:3], v1 offset1:16
	ds_read2_b32 v[4:5], v1 offset0:32 offset1:48
	ds_read2_b32 v[6:7], v1 offset0:64 offset1:80
	ds_read2_b32 v[8:9], v1 offset0:96 offset1:112
	ds_read2_b32 v[10:11], v1 offset0:128 offset1:144
	s_waitcnt lgkmcnt(4)
	v_add_f32_e32 v2, 0, v2
	v_add_f32_e32 v2, v2, v3
	s_waitcnt lgkmcnt(3)
	v_add_f32_e32 v2, v2, v4
	v_add_f32_e32 v2, v2, v5
	s_waitcnt lgkmcnt(2)
	v_add_f32_e32 v2, v2, v6
	v_add_f32_e32 v2, v2, v7
	s_waitcnt lgkmcnt(1)
	v_add_f32_e32 v2, v2, v8
	v_add_f32_e32 v4, v2, v9
	ds_read2_b32 v[2:3], v1 offset0:160 offset1:176
	s_waitcnt lgkmcnt(1)
	v_add_f32_e32 v6, v4, v10
	ds_read2_b32 v[4:5], v1 offset0:192 offset1:208
	v_add_f32_e32 v8, v6, v11
	ds_read2_b32 v[6:7], v1 offset0:224 offset1:240
	s_waitcnt lgkmcnt(2)
	v_add_f32_e32 v1, v8, v2
	v_add_f32_e32 v1, v1, v3
	s_waitcnt lgkmcnt(1)
	v_add_f32_e32 v1, v1, v4
	v_add_f32_e32 v1, v1, v5
	s_waitcnt lgkmcnt(0)
	v_add_f32_e32 v1, v1, v6
	v_add_f32_e32 v1, v1, v7
	v_lshl_or_b32 v0, s12, 4, v0
	v_mul_f32_e32 v2, 0x3eb8aa3b, v1
	v_ashrrev_i32_e32 v1, 31, v0
	v_lshl_add_u64 v[0:1], v[0:1], 2, s[10:11]
	global_store_dword v[0:1], v2, off
